# workgroup index taken from (XCC id, arrival rank on that XCC) at kernel start, so every token group's workgroups sit on one XCD whatever the dispatch order (keeps the XCD-local and pair barriers and L
# speedup vs baseline: 1.0032x; 1.0007x over previous
; #define LAS __attribute__((address_space(3)))
; __global__ void __launch_bounds__(NWAVES * 64, 2) mega(Args args) {
;     extern __shared__ __attribute__((aligned(16))) unsigned char lds[];
;     Frame F;
;     F.lds = (LAS unsigned char*)lds;
;     F.MISC = (volatile LAS unsigned*)(F.lds + MISC_OFF);
;     F.tid = threadIdx.x; F.lane = F.tid & 63; { int w_ = __builtin_amdgcn_readfirstlane(F.tid >> 6); asm volatile("" : "+s"(w_)); F.wave = w_; }
;     F.G = gridDim.x; { const int bx = blockIdx.x; F.vcu = (F.G % 8 == 0) ? (bx % 8) * (F.G / 8) + bx / 8 : bx; }
_Z4mega4Args:
	s_load_dwordx2 s[30:31], s[0:1], 0x80
	v_readfirstlane_b32 s3, v0
	s_cmp_lg_u32 s3, 0
	s_cbranch_scc1 .Lrm_wait
	s_getreg_b32 s4, hwreg(HW_REG_XCC_ID, 0, 4)
	s_and_b32 s4, s4, 15
	s_lshl_b32 s5, s4, 8
	s_add_i32 s5, s5, 0x8800
	s_mov_b64 s[6:7], exec
	s_mov_b64 exec, 1
	v_mov_b32_e32 v1, s5
	v_mov_b32_e32 v2, 1
	s_waitcnt lgkmcnt(0)
	global_atomic_add v1, v1, v2, s[30:31] sc0
	s_waitcnt vmcnt(0)
	v_readfirstlane_b32 s5, v1
	s_lshl_b32 s5, s5, 3
	s_add_i32 s5, s5, s4
	v_mov_b32_e32 v1, s5
	v_mov_b32_e32 v2, 0x27d00
	ds_write_b32 v2, v1
	s_mov_b64 exec, s[6:7]
	s_waitcnt lgkmcnt(0)
.Lrm_wait:
	s_barrier
	v_mov_b32_e32 v1, 0x27d00
	ds_read_b32 v1, v1
	s_waitcnt lgkmcnt(0)
	v_readfirstlane_b32 s2, v1
	s_load_dword s60, s[0:1], 0x90
	v_readfirstlane_b32 s3, v0
	s_lshr_b32 s61, s3, 6
	s_add_u32 s4, s0, 0x90
	s_addc_u32 s5, s1, 0
	s_waitcnt lgkmcnt(0)
	s_and_b32 s3, s60, 7
	v_writelane_b32 v248, s4, 0
	s_cmp_lg_u32 s3, 0
	s_mov_b32 s3, s2
	v_writelane_b32 v248, s5, 1
	s_cbranch_scc0 .LBB0_5
	s_movk_i32 s4, 0x80
	v_cmp_gt_u32_e32 vcc, s4, v0
	s_and_saveexec_b64 s[4:5], vcc
